# speedup vs baseline: 1.0376x; 1.0021x over previous
_Z11gemm_kernelILi256ELi192ELi4ELi2ELi4ELi2ELi2ELi0EEvPKDF16_S1_iiiPDF16_PfPK15HIP_vector_typeIfLj2EE:
	s_load_dwordx8 s[4:11], s[0:1], 0x0
	s_load_dwordx2 s[12:13], s[0:1], 0x30
	s_lshr_b32 s18, s2, 3
	v_readfirstlane_b32 s17, v0
	s_lshr_b32 s14, s17, 6
	s_waitcnt lgkmcnt(0)
	s_ashr_i32 s11, s8, 31
	s_lshr_b32 s3, s11, 22
	s_add_i32 s3, s8, s3
	s_ashr_i32 s15, s3, 10
	s_abs_i32 s16, s15
	v_cvt_f32_u32_e32 v1, s16
	s_sub_i32 s21, 0, s16
	s_mul_hi_i32 s19, s9, 0x2aaaaaab
	s_lshr_b32 s20, s19, 31
	v_rcp_iflag_f32_e32 v1, v1
	s_ashr_i32 s19, s19, 6
	s_add_i32 s19, s19, s20
	s_bfe_u32 s20, s2, 0x20001
	v_mul_f32_e32 v1, 0x4f7ffffe, v1
	v_cvt_u32_f32_e32 v1, v1
	s_ashr_i32 s3, s3, 31
	s_mul_i32 s20, s15, s20
	v_mov_b32_e32 v97, 0
	v_readfirstlane_b32 s22, v1
	s_mul_i32 s21, s21, s22
	s_mul_hi_u32 s21, s22, s21
	s_add_i32 s22, s22, s21
	s_mul_hi_u32 s22, s18, s22
	s_mul_i32 s21, s22, s16
	s_sub_i32 s23, s18, s21
	s_add_i32 s24, s22, 1
	s_sub_i32 s25, s23, s16
	s_cmp_ge_u32 s23, s16
	s_cselect_b32 s22, s24, s22
	s_cselect_b32 s23, s25, s23
	s_add_i32 s24, s22, 1
	s_cmp_ge_u32 s23, s16
	s_cselect_b32 s16, s24, s22
	s_xor_b32 s16, s16, s3
	s_sub_i32 s3, s16, s3
	s_mul_i32 s15, s3, s15
	s_sub_i32 s15, s18, s15
	s_add_i32 s15, s15, s20
	s_bitcmp1_b32 s2, 0
	v_bfe_u32 v1, v0, 3, 3
	s_cselect_b32 s2, s19, 0
	v_lshl_or_b32 v1, s14, 3, v1
	s_add_i32 s18, s3, s2
	s_lshl_b32 s19, s15, 8
	v_lshrrev_b32_e32 v2, 1, v1
	s_lshl_b32 s2, s14, 10
	v_xor_b32_e32 v6, v2, v0
	v_add_u32_e32 v2, s19, v1
	s_cmp_lg_u32 0, -1
	s_mul_i32 s15, s18, 0xc0
	v_ashrrev_i32_e32 v3, 31, v2
	s_cselect_b32 s3, 0, 0
	v_lshlrev_b64 v[2:3], 7, v[2:3]
	v_add_u32_e32 v4, s15, v1
	s_add_i32 s22, s2, s3
	v_lshlrev_b32_e32 v1, 4, v6
	s_lshr_b32 s3, s17, 1
	v_lshl_add_u64 v[2:3], s[4:5], 0, v[2:3]
	v_ashrrev_i32_e32 v5, 31, v4
	v_and_b32_e32 v96, 0x70, v1
	s_add_i32 s24, s22, 0x8000
	s_and_b32 s20, s3, 0x7fffffc0
	v_lshlrev_b64 v[4:5], 7, v[4:5]
	v_lshl_add_u64 v[104:105], v[2:3], 0, v[96:97]
	s_bitcmp1_b32 s17, 6
	s_mov_b64 s[4:5], 0x2000
	s_mov_b32 m0, s22
	s_nop 0
	global_load_lds_dwordx4 v[104:105], off
	v_lshl_add_u64 v[4:5], s[6:7], 0, v[4:5]
	s_cselect_b32 s16, 0x60, 0
	v_lshl_add_u64 v[110:111], v[104:105], 0, s[4:5]
	s_mov_b64 s[6:7], 0x4000
	s_add_i32 s3, s22, 0x2000
	s_mov_b32 m0, s3
	s_nop 0
	global_load_lds_dwordx4 v[110:111], off
	v_lshl_add_u64 v[108:109], v[104:105], 0, s[6:7]
	s_mov_b64 s[26:27], 0x6000
	s_add_i32 s3, s22, 0x4000
	s_mov_b32 m0, s3
	s_nop 0
	global_load_lds_dwordx4 v[108:109], off
	v_lshl_add_u64 v[106:107], v[104:105], 0, s[26:27]
	s_add_i32 s3, s22, 0x6000
	s_mov_b32 m0, s3
	s_nop 0
	global_load_lds_dwordx4 v[106:107], off
	v_lshl_add_u64 v[98:99], v[4:5], 0, v[96:97]
	s_mov_b32 m0, s24
	s_nop 0
	global_load_lds_dwordx4 v[98:99], off
	v_lshl_add_u64 v[100:101], v[98:99], 0, s[4:5]
	s_add_i32 s3, s22, 0xa000
	s_mov_b32 m0, s3
	s_nop 0
	global_load_lds_dwordx4 v[100:101], off
	v_lshl_add_u64 v[102:103], v[98:99], 0, s[6:7]
	s_add_i32 s3, s22, 0xc000
	s_mov_b32 m0, s3
	s_nop 0
	global_load_lds_dwordx4 v[102:103], off
	s_mov_b32 s21, 1
	s_mov_b32 s23, 0
	s_cmp_lt_i32 s10, 64
	v_mov_b32_e32 v96, v97
	v_mov_b32_e32 v95, v97
	v_mov_b32_e32 v94, v97
	v_mov_b32_e32 v93, v97
	v_mov_b32_e32 v92, v97
	v_mov_b32_e32 v91, v97
	v_mov_b32_e32 v90, v97
	v_mov_b32_e32 v89, v97
	v_mov_b32_e32 v88, v97
	v_mov_b32_e32 v87, v97
	v_mov_b32_e32 v86, v97
	v_mov_b32_e32 v85, v97
	v_mov_b32_e32 v84, v97
	v_mov_b32_e32 v83, v97
	v_mov_b32_e32 v82, v97
	v_mov_b32_e32 v81, v97
	v_mov_b32_e32 v80, v97
	v_mov_b32_e32 v79, v97
	v_mov_b32_e32 v78, v97
	v_mov_b32_e32 v77, v97
	v_mov_b32_e32 v76, v97
	v_mov_b32_e32 v75, v97
	v_mov_b32_e32 v74, v97
	v_mov_b32_e32 v73, v97
	v_mov_b32_e32 v72, v97
	v_mov_b32_e32 v71, v97
	v_mov_b32_e32 v70, v97
	v_mov_b32_e32 v69, v97
	v_mov_b32_e32 v68, v97
	v_mov_b32_e32 v67, v97
	v_mov_b32_e32 v66, v97
	v_mov_b32_e32 v65, v97
	v_mov_b32_e32 v64, v97
	v_mov_b32_e32 v63, v97
	v_mov_b32_e32 v62, v97
	v_mov_b32_e32 v61, v97
	v_mov_b32_e32 v60, v97
	v_mov_b32_e32 v59, v97
	v_mov_b32_e32 v58, v97
	v_mov_b32_e32 v57, v97
	v_mov_b32_e32 v56, v97
	v_mov_b32_e32 v55, v97
	v_mov_b32_e32 v54, v97
	v_mov_b32_e32 v53, v97
	v_mov_b32_e32 v52, v97
	v_mov_b32_e32 v51, v97
	v_mov_b32_e32 v50, v97
	v_mov_b32_e32 v49, v97
	v_mov_b32_e32 v48, v97
	v_mov_b32_e32 v47, v97
	v_mov_b32_e32 v46, v97
	v_mov_b32_e32 v45, v97
	v_mov_b32_e32 v44, v97
	v_mov_b32_e32 v43, v97
	v_mov_b32_e32 v42, v97
	v_mov_b32_e32 v41, v97
	v_mov_b32_e32 v40, v97
	v_mov_b32_e32 v39, v97
	v_mov_b32_e32 v38, v97
	v_mov_b32_e32 v37, v97
	v_mov_b32_e32 v36, v97
	v_mov_b32_e32 v35, v97
	v_mov_b32_e32 v34, v97
	v_mov_b32_e32 v33, v97
	v_mov_b32_e32 v32, v97
	v_mov_b32_e32 v31, v97
	v_mov_b32_e32 v30, v97
	v_mov_b32_e32 v29, v97
	v_mov_b32_e32 v28, v97
	v_mov_b32_e32 v27, v97
	v_mov_b32_e32 v26, v97
	v_mov_b32_e32 v25, v97
	v_mov_b32_e32 v24, v97
	v_mov_b32_e32 v23, v97
	v_mov_b32_e32 v22, v97
	v_mov_b32_e32 v21, v97
	v_mov_b32_e32 v20, v97
	v_mov_b32_e32 v19, v97
	v_mov_b32_e32 v18, v97
	v_mov_b32_e32 v17, v97
	v_mov_b32_e32 v16, v97
	v_mov_b32_e32 v15, v97
	v_mov_b32_e32 v14, v97
	v_mov_b32_e32 v13, v97
	v_mov_b32_e32 v12, v97
	v_mov_b32_e32 v11, v97
	v_mov_b32_e32 v10, v97
	v_mov_b32_e32 v9, v97
	v_mov_b32_e32 v8, v97
	v_mov_b32_e32 v7, v97
	v_mov_b32_e32 v6, v97
	v_mov_b32_e32 v5, v97
	v_mov_b32_e32 v4, v97
	v_mov_b32_e32 v3, v97
	v_mov_b32_e32 v2, v97
	v_and_b32_e32 v162, 31, v0
	v_bfe_u32 v1, v0, 5, 1
	s_cbranch_scc1 .LBB2_6
	s_ashr_i32 s3, s10, 31
	s_lshr_b32 s3, s3, 26
	s_add_i32 s3, s10, s3
	v_lshrrev_b32_e32 v2, 1, v0
	s_ashr_i32 s25, s3, 6
	v_bitop3_b32 v2, v1, v2, 7 bitop3:0x78
	s_cmp_lg_u32 0, -1
	v_lshlrev_b32_e32 v120, 4, v2
	v_or_b32_e32 v2, s20, v162
	s_cselect_b32 s3, 0, 0
	v_lshl_add_u32 v121, v2, 7, 0
	v_or_b32_e32 v2, s16, v162
	s_mov_b32 s10, s8
	s_add_i32 s8, s3, s2
	s_ashr_i32 s3, s9, 31
	s_mov_b32 s2, s9
	v_lshl_add_u32 v122, v2, 7, 0
	s_lshl_b64 s[2:3], s[2:3], 7
	v_mov_b32_e32 v2, 0
	s_addk_i32 s8, 0x6000
	v_xor_b32_e32 v123, 32, v120
	v_xor_b32_e32 v124, 64, v120
	v_xor_b32_e32 v125, 0x60, v120
	s_lshl_b64 s[4:5], s[10:11], 7
	s_mov_b64 s[6:7], s[2:3]
	s_mov_b32 s9, 0
	v_mov_b32_e32 v3, v2
	v_mov_b32_e32 v4, v2
	v_mov_b32_e32 v5, v2
	v_mov_b32_e32 v6, v2
	v_mov_b32_e32 v7, v2
	v_mov_b32_e32 v8, v2
	v_mov_b32_e32 v9, v2
	v_mov_b32_e32 v10, v2
	v_mov_b32_e32 v11, v2
	v_mov_b32_e32 v12, v2
	v_mov_b32_e32 v13, v2
	v_mov_b32_e32 v14, v2
	v_mov_b32_e32 v15, v2
	v_mov_b32_e32 v16, v2
	v_mov_b32_e32 v17, v2
	v_mov_b32_e32 v18, v2
	v_mov_b32_e32 v19, v2
	v_mov_b32_e32 v20, v2
	v_mov_b32_e32 v21, v2
	v_mov_b32_e32 v22, v2
	v_mov_b32_e32 v23, v2
	v_mov_b32_e32 v24, v2
	v_mov_b32_e32 v25, v2
	v_mov_b32_e32 v26, v2
	v_mov_b32_e32 v27, v2
	v_mov_b32_e32 v28, v2
	v_mov_b32_e32 v29, v2
	v_mov_b32_e32 v30, v2
	v_mov_b32_e32 v31, v2
	v_mov_b32_e32 v32, v2
	v_mov_b32_e32 v33, v2
	v_mov_b32_e32 v34, v2
	v_mov_b32_e32 v35, v2
	v_mov_b32_e32 v36, v2
	v_mov_b32_e32 v37, v2
	v_mov_b32_e32 v38, v2
	v_mov_b32_e32 v39, v2
	v_mov_b32_e32 v40, v2
	v_mov_b32_e32 v41, v2
	v_mov_b32_e32 v42, v2
	v_mov_b32_e32 v43, v2
	v_mov_b32_e32 v44, v2
	v_mov_b32_e32 v45, v2
	v_mov_b32_e32 v46, v2
	v_mov_b32_e32 v47, v2
	v_mov_b32_e32 v48, v2
	v_mov_b32_e32 v49, v2
	v_mov_b32_e32 v50, v2
	v_mov_b32_e32 v51, v2
	v_mov_b32_e32 v52, v2
	v_mov_b32_e32 v53, v2
	v_mov_b32_e32 v54, v2
	v_mov_b32_e32 v55, v2
	v_mov_b32_e32 v56, v2
	v_mov_b32_e32 v57, v2
	v_mov_b32_e32 v58, v2
	v_mov_b32_e32 v59, v2
	v_mov_b32_e32 v60, v2
	v_mov_b32_e32 v61, v2
	v_mov_b32_e32 v62, v2
	v_mov_b32_e32 v63, v2
	v_mov_b32_e32 v64, v2
	v_mov_b32_e32 v65, v2
	v_mov_b32_e32 v66, v2
	v_mov_b32_e32 v67, v2
	v_mov_b32_e32 v68, v2
	v_mov_b32_e32 v69, v2
	v_mov_b32_e32 v70, v2
	v_mov_b32_e32 v71, v2
	v_mov_b32_e32 v72, v2
	v_mov_b32_e32 v73, v2
	v_mov_b32_e32 v74, v2
	v_mov_b32_e32 v75, v2
	v_mov_b32_e32 v76, v2
	v_mov_b32_e32 v77, v2
	v_mov_b32_e32 v78, v2
	v_mov_b32_e32 v79, v2
	v_mov_b32_e32 v80, v2
	v_mov_b32_e32 v81, v2
	v_mov_b32_e32 v82, v2
	v_mov_b32_e32 v83, v2
	v_mov_b32_e32 v84, v2
	v_mov_b32_e32 v85, v2
	v_mov_b32_e32 v86, v2
	v_mov_b32_e32 v87, v2
	v_mov_b32_e32 v88, v2
	v_mov_b32_e32 v89, v2
	v_mov_b32_e32 v90, v2
	v_mov_b32_e32 v91, v2
	v_mov_b32_e32 v92, v2
	v_mov_b32_e32 v93, v2
	v_mov_b32_e32 v94, v2
	v_mov_b32_e32 v95, v2
	v_mov_b32_e32 v96, v2
	v_mov_b32_e32 v97, v2
	v_lshl_add_u64 v[168:169], v[104:105], 0, s[4:5]
	v_lshl_add_u64 v[170:171], v[110:111], 0, s[4:5]
	v_lshl_add_u64 v[172:173], v[108:109], 0, s[4:5]
	v_lshl_add_u64 v[174:175], v[106:107], 0, s[4:5]
	v_lshl_add_u64 v[176:177], v[98:99], 0, s[2:3]
	v_lshl_add_u64 v[178:179], v[100:101], 0, s[2:3]
	v_lshl_add_u64 v[180:181], v[102:103], 0, s[2:3]
	s_mov_b32 s9, 1
	s_add_i32 s25, s25, -1
	s_cmp_ge_u32 s14, 4
	s_cbranch_scc1 .Lqkv_a0
	s_waitcnt vmcnt(0) lgkmcnt(0)
	s_barrier
	s_mul_i32 s10, s23, 0xe000
	s_mul_i32 s11, s21, 0xe000
	v_add_u32_e32 v142, s10, v122
	v_add_u32_e32 v143, s10, v121
	s_add_i32 s11, s11, s22
	s_xor_b32 s23, s23, 1
	s_xor_b32 s21, s21, 1
	v_add_u32_e32 v144, v142, v120
	v_add_u32_e32 v145, v143, v120
	ds_read_b128 v[130:133], v145
	ds_read_b128 v[104:107], v144 offset:32768
	ds_read_b128 v[108:111], v144 offset:36864
	ds_read_b128 v[134:137], v145 offset:4096
	ds_read_b128 v[126:129], v144 offset:40960
	s_mov_b32 m0, s11
	s_nop 0
	global_load_lds_dwordx4 v[168:169], off
	v_lshl_add_u64 v[168:169], v[168:169], 0, s[4:5]
	s_add_i32 m0, s11, 0x2000
	s_nop 0
	global_load_lds_dwordx4 v[170:171], off
	v_lshl_add_u64 v[170:171], v[170:171], 0, s[4:5]
	s_add_i32 m0, s11, 0x4000
	s_nop 0
	global_load_lds_dwordx4 v[172:173], off
	v_lshl_add_u64 v[172:173], v[172:173], 0, s[4:5]
	v_add_u32_e32 v146, v142, v123
	v_add_u32_e32 v147, v143, v123
	ds_read_b128 v[182:185], v147
	ds_read_b128 v[138:141], v146 offset:32768
	ds_read_b128 v[112:115], v146 offset:36864
	ds_read_b128 v[186:189], v147 offset:4096
	ds_read_b128 v[116:119], v146 offset:40960
	s_waitcnt lgkmcnt(8)
	s_add_i32 m0, s11, 0x6000
	v_mfma_f32_32x32x16_f16 v[82:97], v[104:107], v[130:133], v[82:97]
	global_load_lds_dwordx4 v[174:175], off
	v_lshl_add_u64 v[174:175], v[174:175], 0, s[4:5]
	s_waitcnt lgkmcnt(7)
	v_mfma_f32_32x32x16_f16 v[66:81], v[108:111], v[130:133], v[66:81]
	s_waitcnt lgkmcnt(6)
	s_add_i32 m0, s11, 0x8000
	v_mfma_f32_32x32x16_f16 v[34:49], v[104:107], v[134:137], v[34:49]
	global_load_lds_dwordx4 v[176:177], off
	v_lshl_add_u64 v[176:177], v[176:177], 0, s[2:3]
	v_mfma_f32_32x32x16_f16 v[18:33], v[108:111], v[134:137], v[18:33]
	s_waitcnt lgkmcnt(5)
	s_add_i32 m0, s11, 0xa000
	v_mfma_f32_32x32x16_f16 v[50:65], v[126:129], v[130:133], v[50:65]
	global_load_lds_dwordx4 v[178:179], off
	v_lshl_add_u64 v[178:179], v[178:179], 0, s[2:3]
	v_mfma_f32_32x32x16_f16 v[2:17], v[126:129], v[134:137], v[2:17]
	v_add_u32_e32 v144, v142, v124
	v_add_u32_e32 v145, v143, v124
	ds_read_b128 v[130:133], v145
	ds_read_b128 v[104:107], v144 offset:32768
	ds_read_b128 v[108:111], v144 offset:36864
	ds_read_b128 v[134:137], v145 offset:4096
	ds_read_b128 v[126:129], v144 offset:40960
	s_waitcnt lgkmcnt(8)
	s_add_i32 m0, s11, 0xc000
	v_mfma_f32_32x32x16_f16 v[82:97], v[138:141], v[182:185], v[82:97]
	global_load_lds_dwordx4 v[180:181], off
	v_lshl_add_u64 v[180:181], v[180:181], 0, s[2:3]
	s_waitcnt lgkmcnt(7)
	v_mfma_f32_32x32x16_f16 v[66:81], v[112:115], v[182:185], v[66:81]
	s_waitcnt lgkmcnt(6)
	v_mfma_f32_32x32x16_f16 v[34:49], v[138:141], v[186:189], v[34:49]
	v_mfma_f32_32x32x16_f16 v[18:33], v[112:115], v[186:189], v[18:33]
	s_waitcnt lgkmcnt(5)
	v_mfma_f32_32x32x16_f16 v[50:65], v[116:119], v[182:185], v[50:65]
	v_mfma_f32_32x32x16_f16 v[2:17], v[116:119], v[186:189], v[2:17]
	v_add_u32_e32 v146, v142, v125
	v_add_u32_e32 v147, v143, v125
	ds_read_b128 v[182:185], v147
	ds_read_b128 v[138:141], v146 offset:32768
	ds_read_b128 v[112:115], v146 offset:36864
	ds_read_b128 v[186:189], v147 offset:4096
	ds_read_b128 v[116:119], v146 offset:40960
	s_waitcnt lgkmcnt(8)
	v_mfma_f32_32x32x16_f16 v[82:97], v[104:107], v[130:133], v[82:97]
	s_waitcnt lgkmcnt(7)
	v_mfma_f32_32x32x16_f16 v[66:81], v[108:111], v[130:133], v[66:81]
	s_waitcnt lgkmcnt(6)
	v_mfma_f32_32x32x16_f16 v[34:49], v[104:107], v[134:137], v[34:49]
	v_mfma_f32_32x32x16_f16 v[18:33], v[108:111], v[134:137], v[18:33]
	s_waitcnt lgkmcnt(5)
	v_mfma_f32_32x32x16_f16 v[50:65], v[126:129], v[130:133], v[50:65]
	v_mfma_f32_32x32x16_f16 v[2:17], v[126:129], v[134:137], v[2:17]
